# baseline (speedup 1.0000x reference)
.Lg1_loop:
	s_add_i32 s18, s16, 3
	s_lshl_b32 s18, s18, 7
	s_add_u32 s22, s12, s18
	s_addc_u32 s23, s13, 0
	s_add_u32 s24, s14, s18
	s_addc_u32 s25, s15, 0
	s_add_i32 s26, s17, s20
	s_add_i32 s30, s26, s29
	s_add_i32 s27, s17, 0xd000
	s_cmp_lg_u32 s27, 0x27000
	s_cselect_b32 s27, s27, 0
	s_waitcnt lgkmcnt(0)
	v_mfma_f32_16x16x32_f16 v[34:37], v[116:119], v[100:103], v[34:37]
	ds_read_b128 v[152:155], v94
	v_mfma_f32_16x16x32_f16 v[78:81], v[120:123], v[100:103], v[78:81]
	ds_read_b128 v[136:139], v92
	v_mfma_f32_16x16x32_f16 v[74:77], v[124:127], v[100:103], v[74:77]
	ds_read_b128 v[156:159], v94 offset:2048
	v_mfma_f32_16x16x32_f16 v[70:73], v[128:131], v[100:103], v[70:73]
	ds_read_b128 v[140:143], v92 offset:2048
	v_mfma_f32_16x16x32_f16 v[62:65], v[132:135], v[100:103], v[62:65]
	ds_read_b128 v[160:163], v94 offset:4096
	v_mfma_f32_16x16x32_f16 v[58:61], v[116:119], v[104:107], v[58:61]
	ds_read_b128 v[144:147], v92 offset:4096
	v_mfma_f32_16x16x32_f16 v[54:57], v[120:123], v[104:107], v[54:57]
	ds_read_b128 v[164:167], v94 offset:6144
	v_mfma_f32_16x16x32_f16 v[50:53], v[124:127], v[104:107], v[50:53]
	ds_read_b128 v[148:151], v92 offset:6144
	v_mfma_f32_16x16x32_f16 v[46:49], v[128:131], v[104:107], v[46:49]
	ds_read_b128 v[168:171], v94 offset:8192
	v_mfma_f32_16x16x32_f16 v[42:45], v[132:135], v[104:107], v[42:45]
	v_mfma_f32_16x16x32_f16 v[38:41], v[116:119], v[108:111], v[38:41]
	v_add_u32_e32 v91, s27, v89
	v_mfma_f32_16x16x32_f16 v[30:33], v[120:123], v[108:111], v[30:33]
	v_mfma_f32_16x16x32_f16 v[26:29], v[124:127], v[108:111], v[26:29]
	v_add_u32_e32 v93, s27, v90
	v_mfma_f32_16x16x32_f16 v[22:25], v[128:131], v[108:111], v[22:25]
	v_mfma_f32_16x16x32_f16 v[18:21], v[132:135], v[108:111], v[18:21]
	v_xor_b32_e32 v92, 64, v91
	v_mfma_f32_16x16x32_f16 v[14:17], v[116:119], v[112:115], v[14:17]
	v_mfma_f32_16x16x32_f16 v[10:13], v[120:123], v[112:115], v[10:13]
	v_xor_b32_e32 v94, 64, v93
	v_mfma_f32_16x16x32_f16 v[2:5], v[124:127], v[112:115], v[2:5]
	v_mfma_f32_16x16x32_f16 v[6:9], v[128:131], v[112:115], v[6:9]
	v_mfma_f32_16x16x32_f16 v[66:69], v[132:135], v[112:115], v[66:69]
	s_waitcnt vmcnt(7)
	s_waitcnt lgkmcnt(0)
	s_barrier
	v_mfma_f32_16x16x32_f16 v[34:37], v[152:155], v[136:139], v[34:37]
	ds_read_b128 v[116:119], v93
	v_mfma_f32_16x16x32_f16 v[78:81], v[156:159], v[136:139], v[78:81]
	ds_read_b128 v[100:103], v91
	v_mfma_f32_16x16x32_f16 v[74:77], v[160:163], v[136:139], v[74:77]
	ds_read_b128 v[120:123], v93 offset:2048
	v_mfma_f32_16x16x32_f16 v[70:73], v[164:167], v[136:139], v[70:73]
	ds_read_b128 v[104:107], v91 offset:2048
	v_mfma_f32_16x16x32_f16 v[62:65], v[168:171], v[136:139], v[62:65]
	ds_read_b128 v[124:127], v93 offset:4096
	v_mfma_f32_16x16x32_f16 v[58:61], v[152:155], v[140:143], v[58:61]
	ds_read_b128 v[108:111], v91 offset:4096
	v_mfma_f32_16x16x32_f16 v[54:57], v[156:159], v[140:143], v[54:57]
	ds_read_b128 v[128:131], v93 offset:6144
	v_mfma_f32_16x16x32_f16 v[50:53], v[160:163], v[140:143], v[50:53]
	ds_read_b128 v[112:115], v91 offset:6144
	v_mfma_f32_16x16x32_f16 v[46:49], v[164:167], v[140:143], v[46:49]
	ds_read_b128 v[132:135], v93 offset:8192
	v_mfma_f32_16x16x32_f16 v[42:45], v[168:171], v[140:143], v[42:45]
	v_mfma_f32_16x16x32_f16 v[38:41], v[152:155], v[144:147], v[38:41]
	s_mov_b32 m0, s26
	s_add_i32 s26, s26, 0x2000
	global_load_lds_dwordx4 v82, s[22:23]
	v_mfma_f32_16x16x32_f16 v[30:33], v[156:159], v[144:147], v[30:33]
	s_mov_b32 m0, s26
	s_add_i32 s26, s26, 0x2000
	global_load_lds_dwordx4 v83, s[22:23]
	v_mfma_f32_16x16x32_f16 v[26:29], v[160:163], v[144:147], v[26:29]
	s_mov_b32 m0, s26
	s_add_i32 s26, s26, 0x2000
	global_load_lds_dwordx4 v84, s[22:23]
	v_mfma_f32_16x16x32_f16 v[22:25], v[164:167], v[144:147], v[22:25]
	s_mov_b32 m0, s26
	s_add_i32 s26, s26, 0x2000
	global_load_lds_dwordx4 v85, s[22:23]
	v_mfma_f32_16x16x32_f16 v[18:21], v[168:171], v[144:147], v[18:21]
	s_mov_b32 m0, s26
	s_add_i32 s26, s26, 0x2000
	global_load_lds_dwordx4 v86, s[24:25]
	v_mfma_f32_16x16x32_f16 v[14:17], v[152:155], v[148:151], v[14:17]
	s_mov_b32 m0, s26
	s_add_i32 s26, s26, 0x2000
	global_load_lds_dwordx4 v87, s[24:25]
	v_mfma_f32_16x16x32_f16 v[10:13], v[156:159], v[148:151], v[10:13]
	s_mov_b32 m0, s30
	s_nop 0
	global_load_lds_dwordx4 v88, s[24:25]
	v_mfma_f32_16x16x32_f16 v[2:5], v[160:163], v[148:151], v[2:5]
	v_mfma_f32_16x16x32_f16 v[6:9], v[164:167], v[148:151], v[6:9]
	v_mfma_f32_16x16x32_f16 v[66:69], v[168:171], v[148:151], v[66:69]
	s_mov_b32 s17, s27
	s_add_i32 s16, s16, 1
	s_cmp_lt_u32 s16, 13
	s_cbranch_scc1 .Lg1_loop
	s_add_i32 s27, s17, 0xd000
	s_cmp_lg_u32 s27, 0x27000
	s_cselect_b32 s27, s27, 0
	s_waitcnt lgkmcnt(0)
	v_mfma_f32_16x16x32_f16 v[34:37], v[116:119], v[100:103], v[34:37]
	ds_read_b128 v[152:155], v94
	v_mfma_f32_16x16x32_f16 v[78:81], v[120:123], v[100:103], v[78:81]
	ds_read_b128 v[136:139], v92
	v_mfma_f32_16x16x32_f16 v[74:77], v[124:127], v[100:103], v[74:77]
	ds_read_b128 v[156:159], v94 offset:2048
	v_mfma_f32_16x16x32_f16 v[70:73], v[128:131], v[100:103], v[70:73]
	ds_read_b128 v[140:143], v92 offset:2048
	v_mfma_f32_16x16x32_f16 v[62:65], v[132:135], v[100:103], v[62:65]
	ds_read_b128 v[160:163], v94 offset:4096
	v_mfma_f32_16x16x32_f16 v[58:61], v[116:119], v[104:107], v[58:61]
	ds_read_b128 v[144:147], v92 offset:4096
	v_mfma_f32_16x16x32_f16 v[54:57], v[120:123], v[104:107], v[54:57]
	ds_read_b128 v[164:167], v94 offset:6144
	v_mfma_f32_16x16x32_f16 v[50:53], v[124:127], v[104:107], v[50:53]
	ds_read_b128 v[148:151], v92 offset:6144
	v_mfma_f32_16x16x32_f16 v[46:49], v[128:131], v[104:107], v[46:49]
	ds_read_b128 v[168:171], v94 offset:8192
	v_mfma_f32_16x16x32_f16 v[42:45], v[132:135], v[104:107], v[42:45]
	v_mfma_f32_16x16x32_f16 v[38:41], v[116:119], v[108:111], v[38:41]
	v_add_u32_e32 v91, s27, v89
	v_mfma_f32_16x16x32_f16 v[30:33], v[120:123], v[108:111], v[30:33]
	v_mfma_f32_16x16x32_f16 v[26:29], v[124:127], v[108:111], v[26:29]
	v_add_u32_e32 v93, s27, v90
	v_mfma_f32_16x16x32_f16 v[22:25], v[128:131], v[108:111], v[22:25]
	v_mfma_f32_16x16x32_f16 v[18:21], v[132:135], v[108:111], v[18:21]
	v_xor_b32_e32 v92, 64, v91
	v_mfma_f32_16x16x32_f16 v[14:17], v[116:119], v[112:115], v[14:17]
	v_mfma_f32_16x16x32_f16 v[10:13], v[120:123], v[112:115], v[10:13]
	v_xor_b32_e32 v94, 64, v93
	v_mfma_f32_16x16x32_f16 v[2:5], v[124:127], v[112:115], v[2:5]
	v_mfma_f32_16x16x32_f16 v[6:9], v[128:131], v[112:115], v[6:9]
	v_mfma_f32_16x16x32_f16 v[66:69], v[132:135], v[112:115], v[66:69]
	s_waitcnt vmcnt(7)
	s_waitcnt lgkmcnt(0)
	s_barrier
	v_mfma_f32_16x16x32_f16 v[34:37], v[152:155], v[136:139], v[34:37]
	ds_read_b128 v[116:119], v93
	v_mfma_f32_16x16x32_f16 v[78:81], v[156:159], v[136:139], v[78:81]
	ds_read_b128 v[100:103], v91
	v_mfma_f32_16x16x32_f16 v[74:77], v[160:163], v[136:139], v[74:77]
	ds_read_b128 v[120:123], v93 offset:2048
	v_mfma_f32_16x16x32_f16 v[70:73], v[164:167], v[136:139], v[70:73]
	ds_read_b128 v[104:107], v91 offset:2048
	v_mfma_f32_16x16x32_f16 v[62:65], v[168:171], v[136:139], v[62:65]
	ds_read_b128 v[124:127], v93 offset:4096
	v_mfma_f32_16x16x32_f16 v[58:61], v[152:155], v[140:143], v[58:61]
	ds_read_b128 v[108:111], v91 offset:4096
	v_mfma_f32_16x16x32_f16 v[54:57], v[156:159], v[140:143], v[54:57]
	ds_read_b128 v[128:131], v93 offset:6144
	v_mfma_f32_16x16x32_f16 v[50:53], v[160:163], v[140:143], v[50:53]
	ds_read_b128 v[112:115], v91 offset:6144
	v_mfma_f32_16x16x32_f16 v[46:49], v[164:167], v[140:143], v[46:49]
	ds_read_b128 v[132:135], v93 offset:8192
	v_mfma_f32_16x16x32_f16 v[42:45], v[168:171], v[140:143], v[42:45]
	v_mfma_f32_16x16x32_f16 v[38:41], v[152:155], v[144:147], v[38:41]
	v_mfma_f32_16x16x32_f16 v[30:33], v[156:159], v[144:147], v[30:33]
	v_mfma_f32_16x16x32_f16 v[26:29], v[160:163], v[144:147], v[26:29]
	v_mfma_f32_16x16x32_f16 v[22:25], v[164:167], v[144:147], v[22:25]
	v_mfma_f32_16x16x32_f16 v[18:21], v[168:171], v[144:147], v[18:21]
	v_mfma_f32_16x16x32_f16 v[14:17], v[152:155], v[148:151], v[14:17]
	v_mfma_f32_16x16x32_f16 v[10:13], v[156:159], v[148:151], v[10:13]
	v_mfma_f32_16x16x32_f16 v[2:5], v[160:163], v[148:151], v[2:5]
	v_mfma_f32_16x16x32_f16 v[6:9], v[164:167], v[148:151], v[6:9]
	v_mfma_f32_16x16x32_f16 v[66:69], v[168:171], v[148:151], v[66:69]
	s_mov_b32 s17, s27
	s_add_i32 s27, s17, 0xd000
	s_cmp_lg_u32 s27, 0x27000
	s_cselect_b32 s27, s27, 0
	s_waitcnt lgkmcnt(0)
	v_mfma_f32_16x16x32_f16 v[34:37], v[116:119], v[100:103], v[34:37]
	ds_read_b128 v[152:155], v94
	v_mfma_f32_16x16x32_f16 v[78:81], v[120:123], v[100:103], v[78:81]
	ds_read_b128 v[136:139], v92
	v_mfma_f32_16x16x32_f16 v[74:77], v[124:127], v[100:103], v[74:77]
	ds_read_b128 v[156:159], v94 offset:2048
	v_mfma_f32_16x16x32_f16 v[70:73], v[128:131], v[100:103], v[70:73]
	ds_read_b128 v[140:143], v92 offset:2048
	v_mfma_f32_16x16x32_f16 v[62:65], v[132:135], v[100:103], v[62:65]
	ds_read_b128 v[160:163], v94 offset:4096
	v_mfma_f32_16x16x32_f16 v[58:61], v[116:119], v[104:107], v[58:61]
	ds_read_b128 v[144:147], v92 offset:4096
	v_mfma_f32_16x16x32_f16 v[54:57], v[120:123], v[104:107], v[54:57]
	ds_read_b128 v[164:167], v94 offset:6144
	v_mfma_f32_16x16x32_f16 v[50:53], v[124:127], v[104:107], v[50:53]
	ds_read_b128 v[148:151], v92 offset:6144
	v_mfma_f32_16x16x32_f16 v[46:49], v[128:131], v[104:107], v[46:49]
	ds_read_b128 v[168:171], v94 offset:8192
	v_mfma_f32_16x16x32_f16 v[42:45], v[132:135], v[104:107], v[42:45]
	v_mfma_f32_16x16x32_f16 v[38:41], v[116:119], v[108:111], v[38:41]
	v_add_u32_e32 v91, s27, v89
	v_mfma_f32_16x16x32_f16 v[30:33], v[120:123], v[108:111], v[30:33]
	v_mfma_f32_16x16x32_f16 v[26:29], v[124:127], v[108:111], v[26:29]
	v_add_u32_e32 v93, s27, v90
	v_mfma_f32_16x16x32_f16 v[22:25], v[128:131], v[108:111], v[22:25]
	v_mfma_f32_16x16x32_f16 v[18:21], v[132:135], v[108:111], v[18:21]
	v_xor_b32_e32 v92, 64, v91
	v_mfma_f32_16x16x32_f16 v[14:17], v[116:119], v[112:115], v[14:17]
	v_mfma_f32_16x16x32_f16 v[10:13], v[120:123], v[112:115], v[10:13]
	v_xor_b32_e32 v94, 64, v93
	v_mfma_f32_16x16x32_f16 v[2:5], v[124:127], v[112:115], v[2:5]
	v_mfma_f32_16x16x32_f16 v[6:9], v[128:131], v[112:115], v[6:9]
	v_mfma_f32_16x16x32_f16 v[66:69], v[132:135], v[112:115], v[66:69]
	s_waitcnt vmcnt(0)
	s_waitcnt lgkmcnt(0)
	s_barrier
	v_mfma_f32_16x16x32_f16 v[34:37], v[152:155], v[136:139], v[34:37]
	ds_read_b128 v[116:119], v93
	v_mfma_f32_16x16x32_f16 v[78:81], v[156:159], v[136:139], v[78:81]
	ds_read_b128 v[100:103], v91
	v_mfma_f32_16x16x32_f16 v[74:77], v[160:163], v[136:139], v[74:77]
	ds_read_b128 v[120:123], v93 offset:2048
	v_mfma_f32_16x16x32_f16 v[70:73], v[164:167], v[136:139], v[70:73]
	ds_read_b128 v[104:107], v91 offset:2048
	v_mfma_f32_16x16x32_f16 v[62:65], v[168:171], v[136:139], v[62:65]
	ds_read_b128 v[124:127], v93 offset:4096
	v_mfma_f32_16x16x32_f16 v[58:61], v[152:155], v[140:143], v[58:61]
	ds_read_b128 v[108:111], v91 offset:4096
	v_mfma_f32_16x16x32_f16 v[54:57], v[156:159], v[140:143], v[54:57]
	ds_read_b128 v[128:131], v93 offset:6144
	v_mfma_f32_16x16x32_f16 v[50:53], v[160:163], v[140:143], v[50:53]
	ds_read_b128 v[112:115], v91 offset:6144
	v_mfma_f32_16x16x32_f16 v[46:49], v[164:167], v[140:143], v[46:49]
	ds_read_b128 v[132:135], v93 offset:8192
	v_mfma_f32_16x16x32_f16 v[42:45], v[168:171], v[140:143], v[42:45]
	v_mfma_f32_16x16x32_f16 v[38:41], v[152:155], v[144:147], v[38:41]
	v_mfma_f32_16x16x32_f16 v[30:33], v[156:159], v[144:147], v[30:33]
	v_mfma_f32_16x16x32_f16 v[26:29], v[160:163], v[144:147], v[26:29]
	v_mfma_f32_16x16x32_f16 v[22:25], v[164:167], v[144:147], v[22:25]
	v_mfma_f32_16x16x32_f16 v[18:21], v[168:171], v[144:147], v[18:21]
	v_mfma_f32_16x16x32_f16 v[14:17], v[152:155], v[148:151], v[14:17]
	v_mfma_f32_16x16x32_f16 v[10:13], v[156:159], v[148:151], v[10:13]
	v_mfma_f32_16x16x32_f16 v[2:5], v[160:163], v[148:151], v[2:5]
	v_mfma_f32_16x16x32_f16 v[6:9], v[164:167], v[148:151], v[6:9]
	v_mfma_f32_16x16x32_f16 v[66:69], v[168:171], v[148:151], v[66:69]
	s_mov_b32 s17, s27
	s_add_i32 s27, s17, 0xd000
	s_cmp_lg_u32 s27, 0x27000
	s_cselect_b32 s27, s27, 0
	s_waitcnt lgkmcnt(0)
	v_mfma_f32_16x16x32_f16 v[34:37], v[116:119], v[100:103], v[34:37]
	ds_read_b128 v[152:155], v94
	v_mfma_f32_16x16x32_f16 v[78:81], v[120:123], v[100:103], v[78:81]
	ds_read_b128 v[136:139], v92
	v_mfma_f32_16x16x32_f16 v[74:77], v[124:127], v[100:103], v[74:77]
	ds_read_b128 v[156:159], v94 offset:2048
	v_mfma_f32_16x16x32_f16 v[70:73], v[128:131], v[100:103], v[70:73]
	ds_read_b128 v[140:143], v92 offset:2048
	v_mfma_f32_16x16x32_f16 v[62:65], v[132:135], v[100:103], v[62:65]
	ds_read_b128 v[160:163], v94 offset:4096
	v_mfma_f32_16x16x32_f16 v[58:61], v[116:119], v[104:107], v[58:61]
	ds_read_b128 v[144:147], v92 offset:4096
	v_mfma_f32_16x16x32_f16 v[54:57], v[120:123], v[104:107], v[54:57]
	ds_read_b128 v[164:167], v94 offset:6144
	v_mfma_f32_16x16x32_f16 v[50:53], v[124:127], v[104:107], v[50:53]
	ds_read_b128 v[148:151], v92 offset:6144
	v_mfma_f32_16x16x32_f16 v[46:49], v[128:131], v[104:107], v[46:49]
	ds_read_b128 v[168:171], v94 offset:8192
	v_mfma_f32_16x16x32_f16 v[42:45], v[132:135], v[104:107], v[42:45]
	v_mfma_f32_16x16x32_f16 v[38:41], v[116:119], v[108:111], v[38:41]
	v_add_u32_e32 v91, s27, v89
	v_mfma_f32_16x16x32_f16 v[30:33], v[120:123], v[108:111], v[30:33]
	v_mfma_f32_16x16x32_f16 v[26:29], v[124:127], v[108:111], v[26:29]
	v_add_u32_e32 v93, s27, v90
	v_mfma_f32_16x16x32_f16 v[22:25], v[128:131], v[108:111], v[22:25]
	v_mfma_f32_16x16x32_f16 v[18:21], v[132:135], v[108:111], v[18:21]
	v_xor_b32_e32 v92, 64, v91
	v_mfma_f32_16x16x32_f16 v[14:17], v[116:119], v[112:115], v[14:17]
	v_mfma_f32_16x16x32_f16 v[10:13], v[120:123], v[112:115], v[10:13]
	v_xor_b32_e32 v94, 64, v93
	v_mfma_f32_16x16x32_f16 v[2:5], v[124:127], v[112:115], v[2:5]
	v_mfma_f32_16x16x32_f16 v[6:9], v[128:131], v[112:115], v[6:9]
	v_mfma_f32_16x16x32_f16 v[66:69], v[132:135], v[112:115], v[66:69]
	s_waitcnt lgkmcnt(0)
	s_barrier
	v_mfma_f32_16x16x32_f16 v[34:37], v[152:155], v[136:139], v[34:37]
	ds_read_b128 v[116:119], v93
	v_mfma_f32_16x16x32_f16 v[78:81], v[156:159], v[136:139], v[78:81]
	ds_read_b128 v[100:103], v91
	v_mfma_f32_16x16x32_f16 v[74:77], v[160:163], v[136:139], v[74:77]
	ds_read_b128 v[120:123], v93 offset:2048
	v_mfma_f32_16x16x32_f16 v[70:73], v[164:167], v[136:139], v[70:73]
	ds_read_b128 v[104:107], v91 offset:2048
	v_mfma_f32_16x16x32_f16 v[62:65], v[168:171], v[136:139], v[62:65]
	ds_read_b128 v[124:127], v93 offset:4096
	v_mfma_f32_16x16x32_f16 v[58:61], v[152:155], v[140:143], v[58:61]
	ds_read_b128 v[108:111], v91 offset:4096
	v_mfma_f32_16x16x32_f16 v[54:57], v[156:159], v[140:143], v[54:57]
	ds_read_b128 v[128:131], v93 offset:6144
	v_mfma_f32_16x16x32_f16 v[50:53], v[160:163], v[140:143], v[50:53]
	ds_read_b128 v[112:115], v91 offset:6144
	v_mfma_f32_16x16x32_f16 v[46:49], v[164:167], v[140:143], v[46:49]
	ds_read_b128 v[132:135], v93 offset:8192
	v_mfma_f32_16x16x32_f16 v[42:45], v[168:171], v[140:143], v[42:45]
	v_mfma_f32_16x16x32_f16 v[38:41], v[152:155], v[144:147], v[38:41]
	v_mfma_f32_16x16x32_f16 v[30:33], v[156:159], v[144:147], v[30:33]
	v_mfma_f32_16x16x32_f16 v[26:29], v[160:163], v[144:147], v[26:29]
	v_mfma_f32_16x16x32_f16 v[22:25], v[164:167], v[144:147], v[22:25]
	v_mfma_f32_16x16x32_f16 v[18:21], v[168:171], v[144:147], v[18:21]
	v_mfma_f32_16x16x32_f16 v[14:17], v[152:155], v[148:151], v[14:17]
	v_mfma_f32_16x16x32_f16 v[10:13], v[156:159], v[148:151], v[10:13]
	v_mfma_f32_16x16x32_f16 v[2:5], v[160:163], v[148:151], v[2:5]
	v_mfma_f32_16x16x32_f16 v[6:9], v[164:167], v[148:151], v[6:9]
	v_mfma_f32_16x16x32_f16 v[66:69], v[168:171], v[148:151], v[66:69]
	s_mov_b32 s17, s27
	s_nop 7
